# combine: token B first wait no longer waits for token A's 4 stores (vmcnt 0 -> 4; the two store arms are an if/else, always 4 stores)
# speedup vs baseline: 1.0029x; 1.0021x over previous
; DI void phase_combine(const Frame& F, int l) {
;     ...
;         for (int q = 0; q < 16; ++q) { const int t = t0 + q;
;             f32x4 y[4], x[4], hv[4];
; #pragma unroll
;             for (int j = 0; j < 4; ++j) y[j] = (f32x4){0.f, 0.f, 0.f, 0.f};
;             load_bf16_row((const bf16_t*)(F.ws + WS_XB) + (size_t)t * D, F.lane, x);
; #pragma unroll
;             for (int k = 0; k < 4; ++k) { const int slot = __builtin_amdgcn_readlane(slotv, 4 * q + k); const float gk = __builtin_bit_cast(float, __builtin_amdgcn_readlane(gvi, 4 * q + k)) * ysc;
;                 const unsigned char* rp = (const unsigned char*)(F.ws + WS_XS) + (size_t)slot * D + 8 * F.lane; unsigned w[4];
; #pragma unroll
;                 for (int g = 0; g < 2; ++g) { const u32x2 ww = *(const u32x2*)(rp + 512 * g); w[2 * g] = ww.x; w[2 * g + 1] = ww.y; }
; #pragma unroll
;                 for (int j = 0; j < 4; ++j) { const f32x2 lo = __builtin_amdgcn_cvt_pk_f32_fp8((int)w[j], false), hi = __builtin_amdgcn_cvt_pk_f32_fp8((int)w[j], true); y[j] += (f32x4){lo.x, lo.y, hi.x, hi.y} * gk; } }
.LBB0_1395:
	s_add_i32 s4, s54, 1
	s_ashr_i32 s5, s4, 31
	s_lshl_b64 s[56:57], s[4:5], 10
	s_lshl_b64 s[4:5], s[4:5], 11
	s_add_i32 s2, s22, -3
	v_lshl_add_u64 v[74:75], v[68:69], 0, s[4:5]
	v_readlane_b32 s4, v99, s2
	s_ashr_i32 s5, s4, 31
	s_lshl_b64 s[4:5], s[4:5], 10
	v_lshl_add_u64 v[76:77], v[70:71], 0, s[4:5]
	s_nop 0
	s_add_i32 s66, s22, -2
	v_readlane_b32 s68, v99, s66
	s_ashr_i32 s69, s68, 31
	s_lshl_b64 s[68:69], s[68:69], 10
	v_lshl_add_u64 v[162:163], v[70:71], 0, s[68:69]
	s_add_i32 s66, s22, -1
	v_readlane_b32 s68, v99, s66
	s_ashr_i32 s69, s68, 31
	s_lshl_b64 s[68:69], s[68:69], 10
	v_lshl_add_u64 v[164:165], v[70:71], 0, s[68:69]
	s_add_i32 s66, s22, 0
	v_readlane_b32 s68, v99, s66
	s_ashr_i32 s69, s68, 31
	s_lshl_b64 s[68:69], s[68:69], 10
	v_lshl_add_u64 v[166:167], v[70:71], 0, s[68:69]
	v_readlane_b32 s2, v98, s2
	s_and_b64 vcc, exec, s[36:37]
	s_waitcnt vmcnt(4)
	v_lshlrev_b32_e32 v48, 16, v168
	v_mul_f32_e32 v80, s2, v65
	s_waitcnt vmcnt(4)
	v_cvt_pk_f32_fp8_e32 v[82:83], v176
	v_cvt_pk_f32_fp8_sdwa v[84:85], v176 src0_sel:WORD_1
	v_cvt_pk_f32_fp8_e32 v[86:87], v177
	v_cvt_pk_f32_fp8_sdwa v[78:79], v177 src0_sel:WORD_1
	s_waitcnt vmcnt(4)
	v_cvt_pk_f32_fp8_e32 v[88:89], v178
	v_cvt_pk_f32_fp8_sdwa v[90:91], v178 src0_sel:WORD_1
	v_cvt_pk_f32_fp8_e32 v[92:93], v179
	v_cvt_pk_f32_fp8_sdwa v[76:77], v179 src0_sel:WORD_1
	s_add_i32 s2, s22, -2
	v_readlane_b32 s4, v99, s2
	s_ashr_i32 s5, s4, 31
	s_lshl_b64 s[4:5], s[4:5], 10
	v_pk_fma_f32 v[84:85], v[80:81], v[84:85], 0 op_sel_hi:[0,1,0]
	v_pk_fma_f32 v[82:83], v[80:81], v[82:83], 0 op_sel_hi:[0,1,0]
	v_pk_fma_f32 v[78:79], v[80:81], v[78:79], 0 op_sel_hi:[0,1,0]
	v_pk_fma_f32 v[86:87], v[80:81], v[86:87], 0 op_sel_hi:[0,1,0]
	v_pk_fma_f32 v[88:89], v[80:81], v[88:89], 0 op_sel_hi:[0,1,0]
	v_pk_fma_f32 v[90:91], v[80:81], v[90:91], 0 op_sel_hi:[0,1,0]
	v_pk_fma_f32 v[92:93], v[80:81], v[92:93], 0 op_sel_hi:[0,1,0]
	v_pk_fma_f32 v[76:77], v[80:81], v[76:77], 0 op_sel_hi:[0,1,0]
	v_lshl_add_u64 v[80:81], v[70:71], 0, s[4:5]
	s_nop 0
	v_readlane_b32 s2, v98, s2
	v_and_b32_e32 v49, 0xffff0000, v168
	v_lshlrev_b32_e32 v50, 16, v169
	v_mul_f32_e32 v100, s2, v65
	s_add_i32 s2, s22, -1
	v_readlane_b32 s4, v99, s2
	s_ashr_i32 s5, s4, 31
	s_lshl_b64 s[4:5], s[4:5], 10
	v_readlane_b32 s2, v98, s2
	v_and_b32_e32 v51, 0xffff0000, v169
	v_lshlrev_b32_e32 v52, 16, v170
	v_mul_f32_e32 v106, s2, v65
	v_readlane_b32 s2, v98, s22
	v_and_b32_e32 v53, 0xffff0000, v170
	v_lshlrev_b32_e32 v54, 16, v171
	v_and_b32_e32 v55, 0xffff0000, v171
	v_lshlrev_b32_e32 v56, 16, v172
	v_and_b32_e32 v57, 0xffff0000, v172
	v_lshlrev_b32_e32 v58, 16, v173
	v_and_b32_e32 v59, 0xffff0000, v173
	v_lshlrev_b32_e32 v60, 16, v174
	v_and_b32_e32 v61, 0xffff0000, v174
	v_lshlrev_b32_e32 v62, 16, v175
	v_and_b32_e32 v63, 0xffff0000, v175
	s_waitcnt vmcnt(4)
	v_cvt_pk_f32_fp8_e32 v[102:103], v180
	v_cvt_pk_f32_fp8_sdwa v[104:105], v180 src0_sel:WORD_1
	v_pk_fma_f32 v[82:83], v[100:101], v[102:103], v[82:83] op_sel_hi:[0,1,1]
	v_cvt_pk_f32_fp8_e32 v[102:103], v181
	v_cvt_pk_f32_fp8_sdwa v[94:95], v181 src0_sel:WORD_1
	v_pk_fma_f32 v[84:85], v[100:101], v[104:105], v[84:85] op_sel_hi:[0,1,1]
	v_pk_fma_f32 v[86:87], v[100:101], v[102:103], v[86:87] op_sel_hi:[0,1,1]
	v_pk_fma_f32 v[78:79], v[100:101], v[94:95], v[78:79] op_sel_hi:[0,1,1]
	s_waitcnt vmcnt(4)
	v_cvt_pk_f32_fp8_e32 v[94:95], v182
	v_cvt_pk_f32_fp8_sdwa v[102:103], v182 src0_sel:WORD_1
	v_pk_fma_f32 v[94:95], v[100:101], v[94:95], v[88:89] op_sel_hi:[0,1,1]
	v_cvt_pk_f32_fp8_e32 v[88:89], v183
	v_cvt_pk_f32_fp8_sdwa v[80:81], v183 src0_sel:WORD_1
	v_pk_fma_f32 v[102:103], v[100:101], v[102:103], v[90:91] op_sel_hi:[0,1,1]
	v_pk_fma_f32 v[104:105], v[100:101], v[80:81], v[76:77] op_sel_hi:[0,1,1]
	v_lshl_add_u64 v[80:81], v[70:71], 0, s[4:5]
	v_pk_fma_f32 v[76:77], v[100:101], v[88:89], v[92:93] op_sel_hi:[0,1,1]
	v_readlane_b32 s4, v99, s22
	s_ashr_i32 s5, s4, 31
	s_lshl_b64 s[4:5], s[4:5], 10
	s_waitcnt vmcnt(4)
	v_cvt_pk_f32_fp8_e32 v[80:81], v184
	v_cvt_pk_f32_fp8_sdwa v[88:89], v184 src0_sel:WORD_1
	v_pk_fma_f32 v[90:91], v[106:107], v[80:81], v[82:83] op_sel_hi:[0,1,1]
	v_cvt_pk_f32_fp8_sdwa v[82:83], v185 src0_sel:WORD_1
	v_pk_fma_f32 v[88:89], v[106:107], v[88:89], v[84:85] op_sel_hi:[0,1,1]
	v_cvt_pk_f32_fp8_e32 v[80:81], v185
	s_waitcnt vmcnt(4)
; DI void phase_combine(const Frame& F, int l) {
;     ...
;             for (int k = 0; k < 4; ++k) { const int slot = __builtin_amdgcn_readlane(slotv, 4 * q + k); const float gk = __builtin_bit_cast(float, __builtin_amdgcn_readlane(gvi, 4 * q + k)) * ysc;
;                 const unsigned char* rp = (const unsigned char*)(F.ws + WS_XS) + (size_t)slot * D + 8 * F.lane; unsigned w[4];
; #pragma unroll
;                 for (int g = 0; g < 2; ++g) { const u32x2 ww = *(const u32x2*)(rp + 512 * g); w[2 * g] = ww.x; w[2 * g + 1] = ww.y; }
; #pragma unroll
;                 for (int j = 0; j < 4; ++j) { const f32x2 lo = __builtin_amdgcn_cvt_pk_f32_fp8((int)w[j], false), hi = __builtin_amdgcn_cvt_pk_f32_fp8((int)w[j], true); y[j] += (f32x4){lo.x, lo.y, hi.x, hi.y} * gk; } }
;             const float rstd = rms_rstd(y);
; #pragma unroll
;             for (int j = 0; j < 4; ++j) x[j] = x[j] + Bv[j] * (y[j] * rstd);
	v_cvt_pk_f32_fp8_sdwa v[92:93], v187 src0_sel:WORD_1
	v_pk_fma_f32 v[84:85], v[106:107], v[82:83], v[78:79] op_sel_hi:[0,1,1]
	v_cvt_pk_f32_fp8_e32 v[78:79], v186
	v_pk_fma_f32 v[86:87], v[106:107], v[80:81], v[86:87] op_sel_hi:[0,1,1]
	v_cvt_pk_f32_fp8_sdwa v[82:83], v186 src0_sel:WORD_1
	v_mul_f32_e32 v100, s2, v65
	v_pk_fma_f32 v[80:81], v[106:107], v[78:79], v[94:95] op_sel_hi:[0,1,1]
	v_cvt_pk_f32_fp8_e32 v[78:79], v187
	v_pk_fma_f32 v[82:83], v[106:107], v[82:83], v[102:103] op_sel_hi:[0,1,1]
	v_pk_fma_f32 v[76:77], v[106:107], v[78:79], v[76:77] op_sel_hi:[0,1,1]
	v_pk_fma_f32 v[78:79], v[106:107], v[92:93], v[104:105] op_sel_hi:[0,1,1]
	v_lshl_add_u64 v[92:93], v[70:71], 0, s[4:5]
	s_nop 0
	s_waitcnt vmcnt(4)
	v_cvt_pk_f32_fp8_e32 v[102:103], v188
	v_cvt_pk_f32_fp8_sdwa v[104:105], v188 src0_sel:WORD_1
	v_pk_fma_f32 v[90:91], v[100:101], v[102:103], v[90:91] op_sel_hi:[0,1,1]
	v_cvt_pk_f32_fp8_e32 v[102:103], v189
	v_cvt_pk_f32_fp8_sdwa v[94:95], v189 src0_sel:WORD_1
	v_pk_fma_f32 v[88:89], v[100:101], v[104:105], v[88:89] op_sel_hi:[0,1,1]
	v_pk_fma_f32 v[86:87], v[100:101], v[102:103], v[86:87] op_sel_hi:[0,1,1]
	v_pk_fma_f32 v[84:85], v[100:101], v[94:95], v[84:85] op_sel_hi:[0,1,1]
	s_waitcnt vmcnt(4)
	v_cvt_pk_f32_fp8_e32 v[94:95], v190
	v_cvt_pk_f32_fp8_sdwa v[102:103], v190 src0_sel:WORD_1
	v_pk_fma_f32 v[80:81], v[100:101], v[94:95], v[80:81] op_sel_hi:[0,1,1]
	v_cvt_pk_f32_fp8_e32 v[94:95], v191
	v_cvt_pk_f32_fp8_sdwa v[92:93], v191 src0_sel:WORD_1
	v_pk_fma_f32 v[82:83], v[100:101], v[102:103], v[82:83] op_sel_hi:[0,1,1]
	v_pk_fma_f32 v[76:77], v[100:101], v[94:95], v[76:77] op_sel_hi:[0,1,1]
	v_pk_fma_f32 v[78:79], v[100:101], v[92:93], v[78:79] op_sel_hi:[0,1,1]
	v_pk_mul_f32 v[92:93], v[88:89], v[88:89]
	v_pk_mul_f32 v[94:95], v[90:91], v[90:91]
	s_nop 0
	v_pk_mov_b32 v[100:101], v[94:95], v[92:93] op_sel:[1,0]
	v_mov_b32_e32 v95, v93
	v_pk_add_f32 v[92:93], v[100:101], v[94:95]
	v_pk_mul_f32 v[94:95], v[84:85], v[84:85]
	v_pk_mul_f32 v[100:101], v[86:87], v[86:87]
	v_pk_add_f32 v[92:93], v[92:93], v[92:93] op_sel:[0,1] op_sel_hi:[1,0]
	v_pk_mov_b32 v[102:103], v[100:101], v[94:95] op_sel:[1,0]
	v_mov_b32_e32 v101, v95
	v_pk_add_f32 v[94:95], v[102:103], v[100:101]
	v_mul_f32_e32 v100, v76, v76
	v_mul_f32_e32 v101, v77, v77
	v_pk_add_f32 v[94:95], v[94:95], v[94:95] op_sel:[0,1] op_sel_hi:[1,0]
	v_mov_b32_e32 v93, v100
	v_mov_b32_e32 v95, v101
	v_pk_add_f32 v[92:93], v[92:93], v[94:95]
	v_mul_f32_e32 v94, v81, v81
	v_mul_f32_e32 v100, v83, v83
	v_mul_f32_e32 v102, v78, v78
	v_mul_f32_e32 v103, v79, v79
	v_pk_fma_f32 v[94:95], v[80:81], v[80:81], v[94:95] op_sel_hi:[1,1,0]
	v_pk_fma_f32 v[100:101], v[82:83], v[82:83], v[100:101] op_sel_hi:[1,1,0]
	v_mov_b32_e32 v95, v102
	v_mov_b32_e32 v101, v103
	v_pk_add_f32 v[94:95], v[94:95], v[100:101]
	s_nop 0
	v_pk_add_f32 v[92:93], v[92:93], v[94:95]
	s_nop 0
	v_add_f32_e32 v92, v92, v93
	s_nop 1
	v_add_f32_dpp v92, v92, v92 quad_perm:[1,0,3,2] row_mask:0xf bank_mask:0xf bound_ctrl:1
	s_nop 1
	v_add_f32_dpp v92, v92, v92 quad_perm:[2,3,0,1] row_mask:0xf bank_mask:0xf bound_ctrl:1
	s_nop 1
	v_add_f32_dpp v92, v92, v92 row_half_mirror row_mask:0xf bank_mask:0xf bound_ctrl:1
	s_nop 1
	v_add_f32_dpp v92, v92, v92 row_mirror row_mask:0xf bank_mask:0xf bound_ctrl:1
	s_nop 0
	v_readlane_b32 s2, v92, 16
	v_readlane_b32 s10, v92, 48
	v_readlane_b32 s4, v92, 0
	v_readlane_b32 s5, v92, 32
	v_mov_b32_e32 v92, s2
	v_mov_b32_e32 v93, s10
	v_pk_add_f32 v[92:93], s[4:5], v[92:93]
	s_mov_b64 s[4:5], -1
	v_add_f32_e32 v92, v92, v93
	v_mov_b32_e32 v93, 0x358637bd
	s_nop 0
	v_fmac_f32_e32 v93, 0x3a800000, v92
	v_rsq_f32_e32 v92, v93
	s_nop 0
	v_pk_mul_f32 v[90:91], v[90:91], v[92:93] op_sel_hi:[1,0]
	v_pk_mul_f32 v[88:89], v[88:89], v[92:93] op_sel_hi:[1,0]
	v_pk_mul_f32 v[86:87], v[86:87], v[92:93] op_sel_hi:[1,0]
	v_pk_mul_f32 v[84:85], v[84:85], v[92:93] op_sel_hi:[1,0]
	v_pk_mul_f32 v[80:81], v[80:81], v[92:93] op_sel_hi:[1,0]
	v_pk_mul_f32 v[82:83], v[82:83], v[92:93] op_sel_hi:[1,0]
	v_pk_mul_f32 v[76:77], v[76:77], v[92:93] op_sel_hi:[1,0]
	v_pk_mul_f32 v[78:79], v[78:79], v[92:93] op_sel_hi:[1,0]
	v_pk_fma_f32 v[50:51], v[2:3], v[88:89], v[50:51]
	v_pk_fma_f32 v[48:49], v[0:1], v[90:91], v[48:49]
	v_pk_fma_f32 v[54:55], v[6:7], v[84:85], v[54:55]
	v_pk_fma_f32 v[52:53], v[4:5], v[86:87], v[52:53]
	v_pk_fma_f32 v[58:59], v[10:11], v[82:83], v[58:59]
	v_pk_fma_f32 v[56:57], v[8:9], v[80:81], v[56:57]
	v_pk_fma_f32 v[62:63], v[14:15], v[78:79], v[62:63]
	v_pk_fma_f32 v[60:61], v[12:13], v[76:77], v[60:61]
	s_cbranch_vccz .LBB0_1397
	s_andn2_b64 vcc, exec, s[4:5]
	s_cbranch_vccnz .LBB0_1390
	s_branch .LBB0_1398
